# attention QK^T 3-deep K-fragment LDS ring (strategy 8) re-tested on top of the drain-free per-tile barrier (v41)
# speedup vs baseline: 1.0051x; 1.0050x over previous
; #define LAS __attribute__((address_space(3)))
; #define SBAR() __builtin_amdgcn_sched_barrier(0)
; #define VWRITE(b) do { *(LAS bf16x8*)(V_lds + (b) * SHM_V + vst0) = vs0; *(LAS bf16x8*)(V_lds + (b) * SHM_V + vst1) = vs1; } while (0)
; #define KWAIT_BAR(nv) do { if ((nv) == 2) asm volatile("s_waitcnt vmcnt(2)" ::: "memory"); else asm volatile("s_waitcnt vmcnt(0)" ::: "memory"); __syncthreads(); } while (0)
; #define SWAIT() asm volatile("s_waitcnt vmcnt(0)" ::: "memory")
; __device__ __forceinline__ void qkt(f32x16& p0, f32x16& p1, const LAS char* Kl, const bf16x8* qr, const LAS char* Ql, const f32x16& init) {
; #pragma unroll
;     for (int d0 = 0; d0 < 12; ++d0) {
;         const bf16x8 b0 = *reinterpret_cast<const LAS bf16x8*>(Kl + d0 * 32);
;         const bf16x8 b1 = *reinterpret_cast<const LAS bf16x8*>(Kl + 32 * KROWB + d0 * 32);
;         const bf16x8 q = d0 < NQR ? qr[d0 < NQR ? d0 : 0] : *reinterpret_cast<const LAS bf16x8*>(Ql + (d0 - NQR) * 32);
;         p0 = __builtin_amdgcn_mfma_f32_32x32x16_bf16(b0, q, d0 == 0 ? init : p0, 0, 0, 0);
;         p1 = __builtin_amdgcn_mfma_f32_32x32x16_bf16(b1, q, d0 == 0 ? init : p1, 0, 0, 0); }
; __device__ __forceinline__ void attn_unit(const bf16* __restrict__ Qraw, const float* __restrict__ ssq, const float* __restrict__ qn, int t0, const bf16* __restrict__ Kh, const bf16* __restrict__ Vh, bf16* __restrict__ Ob, int seq, LAS char* lds, int tid) {
;     ...
;         KWAIT_BAR(2);
;     }
;     SWAIT(); VWRITE(1);
;     SBAR(); qkt(pB0, pB1, Kl0 + SHM_K, qr, Ql, negm);
;     finishSM(pA0, pA1, l_reg, pa0, pa1, pa2, pa3); SBAR();
;     pv_d0(o, vb0, pa0, pa1, pa2, pa3); partialSM(pB0, pB1, negm, l_reg, o, al_l, r32, hi);
;     __syncthreads();
;     finishSM(pB0, pB1, l_reg, pa0, pa1, pa2, pa3); SBAR();
;     pv_d0(o, vb0 + SHM_V, pa0, pa1, pa2, pa3);
.LBB0_1470:
	v_exp_f32_e32 v228, v130
	v_exp_f32_e32 v231, v131
	v_exp_f32_e32 v229, v132
	v_exp_f32_e32 v232, v133
	v_exp_f32_e32 v230, v134
	v_exp_f32_e32 v233, v135
	v_exp_f32_e32 v226, v136
	v_exp_f32_e32 v227, v137
	v_exp_f32_e32 v204, v138
	v_exp_f32_e32 v206, v139
	v_exp_f32_e32 v205, v140
	v_exp_f32_e32 v207, v141
	v_exp_f32_e32 v184, v142
	v_exp_f32_e32 v202, v143
	v_exp_f32_e32 v185, v144
	v_exp_f32_e32 v203, v145
	s_waitcnt vmcnt(2)
	s_add_u32 s60, s60, 0xc000
	s_addc_u32 s59, s59, 0
	s_add_i32 s65, s65, 2
	s_cmp_ge_u32 s65, s57
	v_lshl_add_u64 v[182:183], v[182:183], 0, s[16:17]
	s_barrier
	s_cbranch_scc0 .LBB0_1462
	v_mov_b64_e32 v[66:67], v[82:83]
	v_mov_b64_e32 v[68:69], v[84:85]
	v_mov_b64_e32 v[70:71], v[86:87]
	v_mov_b64_e32 v[72:73], v[88:89]
	v_mov_b64_e32 v[74:75], v[90:91]
	v_mov_b64_e32 v[76:77], v[92:93]
	v_mov_b64_e32 v[78:79], v[94:95]
	v_mov_b64_e32 v[80:81], v[96:97]
	s_branch .LBB0_1477
